# tail router: the 8 LDS fragment reads for the 32x32x16 MFMA chain issued together with counted waits
# baseline (speedup 1.0000x reference)
; #define LAS __attribute__((address_space(3)))
; DI unsigned pk2(float lo, float hi) { return f2bf(lo) | (f2bf(hi) << 16); }
; DI unsigned pk_fp8x4(float a, float b, float c, float d) { int p = 0; p = __builtin_amdgcn_cvt_pk_fp8_f32(a, b, p, false); p = __builtin_amdgcn_cvt_pk_fp8_f32(c, d, p, true); return (unsigned)p; }
; DI void phase_tail(const Frame& F, int l) {
;     ...
;         for (int q = 0; q < 4; ++q) {
;             const int tkl = 4 * F.wave + q, t = 32 * ti + tkl;
;             f32x4 y[4], x[4], hv[4];
;             load_bf16_row((const bf16_t*)(F.ws + WS_Y) + (size_t)t * D, F.lane, y);
;             load_bf16_row((const bf16_t*)(F.ws + WS_XB) + (size_t)t * D, F.lane, x);
;             const float rstd = rms_rstd(y);
; #pragma unroll
;             for (int j = 0; j < 4; ++j) x[j] = x[j] + Bv[j] * (y[j] * rstd);
;             store_bf16_row((bf16_t*)(F.ws + WS_XB) + (size_t)t * D, F.lane, x);
;             { const float rs2 = rms_rstd(x);
; #pragma unroll
;               for (int j = 0; j < 4; ++j) hv[j] = x[j] * rs2 * Av[j] + Sv[j];
; #pragma unroll
;               for (int g = 0; g < 2; ++g) { u32x2 w; w.x = pk_fp8x4(hv[2 * g].x, hv[2 * g].y, hv[2 * g].z, hv[2 * g].w); w.y = pk_fp8x4(hv[2 * g + 1].x, hv[2 * g + 1].y, hv[2 * g + 1].z, hv[2 * g + 1].w);
;                   *(u32x2*)((unsigned char*)(F.ws + WS_H8) + (size_t)t * D + 8 * F.lane + 512 * g) = w; } }
; #pragma unroll
;             for (int g = 0; g < 2; ++g) { u32x4 w; w.x = pk2(hv[2 * g].x, hv[2 * g].y); w.y = pk2(hv[2 * g].z, hv[2 * g].w); w.z = pk2(hv[2 * g + 1].x, hv[2 * g + 1].y); w.w = pk2(hv[2 * g + 1].z, hv[2 * g + 1].w);
;                 *(LAS u32x4*)(Ht + tkl * HT_STRIDE + 8 * F.lane + 512 * g) = w; }
.Ltail_pf_it0:
	v_lshl_add_u64 v[100:101], s[54:55], 0, v[62:63]
	v_add_co_u32_e32 v102, vcc, 0x94000000, v100
	s_brev_b32 s2, 23
	s_nop 0
	v_addc_co_u32_e32 v103, vcc, 0, v101, vcc
	v_add_co_u32_e32 v116, vcc, s2, v100
	v_addc_co_u32_e32 v117, vcc, 0, v101, vcc
	s_ashr_i32 s47, s46, 31
	s_lshl_b64 s[66:67], s[46:47], 10
	s_lshl_b64 s[68:69], s[46:47], 11
	v_lshl_add_u64 v[176:177], v[54:55], 0, s[68:69]
	v_lshl_add_u64 v[178:179], v[56:57], 0, s[68:69]
	v_lshl_add_u64 v[62:63], v[62:63], 0, s[0:1]
	s_waitcnt vmcnt(15)
	v_lshlrev_b32_e32 v128, 16, v125
	s_waitcnt vmcnt(14)
	v_lshlrev_b32_e32 v108, 16, v146
	v_and_b32_e32 v143, 0xffff0000, v146
	v_lshlrev_b32_e32 v114, 16, v147
	s_waitcnt vmcnt(13)
	v_lshlrev_b32_e32 v102, 16, v110
	v_and_b32_e32 v103, 0xffff0000, v110
	v_lshlrev_b32_e32 v110, 16, v124
	v_lshlrev_b32_e32 v100, 16, v111
	v_and_b32_e32 v101, 0xffff0000, v111
	v_and_b32_e32 v111, 0xffff0000, v124
	v_mul_f32_e32 v124, v110, v110
	v_and_b32_e32 v115, 0xffff0000, v147
	v_pk_fma_f32 v[146:147], v[110:111], v[110:111], v[124:125] op_sel_hi:[1,1,0]
	v_and_b32_e32 v129, 0xffff0000, v125
	v_mul_f32_e32 v124, v128, v128
	v_pk_fma_f32 v[148:149], v[128:129], v[128:129], v[124:125] op_sel_hi:[1,1,0]
	v_lshlrev_b32_e32 v125, 16, v127
	v_lshlrev_b32_e32 v124, 16, v126
	v_and_b32_e32 v127, 0xffff0000, v127
	v_and_b32_e32 v126, 0xffff0000, v126
	v_pk_mul_f32 v[130:131], v[126:127], v[126:127]
	v_mov_b32_e32 v109, v147
	v_pk_fma_f32 v[130:131], v[124:125], v[124:125], v[130:131]
	v_mov_b32_e32 v154, v108
	v_pk_add_f32 v[150:151], v[130:131], v[130:131] op_sel_hi:[0,1]
	v_lshlrev_b32_e32 v130, 16, v144
	v_and_b32_e32 v131, 0xffff0000, v144
	v_mul_f32_e32 v132, v130, v130
	v_pk_fma_f32 v[152:153], v[130:131], v[130:131], v[132:133] op_sel_hi:[1,1,0]
	v_lshlrev_b32_e32 v132, 16, v145
	v_and_b32_e32 v133, 0xffff0000, v145
	v_mul_f32_e32 v144, v132, v132
	v_mov_b32_e32 v155, v149
	v_pk_fma_f32 v[144:145], v[132:133], v[132:133], v[144:145] op_sel_hi:[1,1,0]
	v_pk_mul_f32 v[154:155], v[108:109], v[154:155]
	v_pk_add_f32 v[146:147], v[146:147], v[148:149]
	v_mul_f32_e32 v150, v143, v143
	v_mul_f32_e32 v152, v114, v114
	v_mul_f32_e32 v144, v115, v115
	v_mov_b32_e32 v155, v147
	v_pk_add_f32 v[146:147], v[154:155], v[150:151]
	v_pk_add_f32 v[144:145], v[152:153], v[144:145]
	v_lshlrev_b32_e32 v106, 16, v112
	v_pk_add_f32 v[144:145], v[146:147], v[144:145]
	v_and_b32_e32 v107, 0xffff0000, v112
	v_add_f32_e32 v109, v144, v145
	s_waitcnt vmcnt(12)
	v_lshlrev_b32_e32 v122, 16, v119
	v_and_b32_e32 v123, 0xffff0000, v119
	v_add_f32_dpp v109, v109, v109 quad_perm:[1,0,3,2] row_mask:0xf bank_mask:0xf bound_ctrl:1
	v_lshlrev_b32_e32 v104, 16, v113
	v_and_b32_e32 v105, 0xffff0000, v113
	v_add_f32_dpp v109, v109, v109 quad_perm:[2,3,0,1] row_mask:0xf bank_mask:0xf bound_ctrl:1
	v_lshlrev_b32_e32 v112, 16, v118
	v_and_b32_e32 v113, 0xffff0000, v118
	v_add_f32_dpp v109, v109, v109 row_half_mirror row_mask:0xf bank_mask:0xf bound_ctrl:1
	v_lshlrev_b32_e32 v118, 16, v120
	v_and_b32_e32 v119, 0xffff0000, v120
	v_add_f32_dpp v109, v109, v109 row_mirror row_mask:0xf bank_mask:0xf bound_ctrl:1
	v_lshlrev_b32_e32 v120, 16, v121
	v_readlane_b32 s2, v109, 16
	v_readlane_b32 s5, v109, 48
	v_readlane_b32 s6, v109, 0
	v_readlane_b32 s7, v109, 32
	v_mov_b32_e32 v144, s2
	v_mov_b32_e32 v145, s5
	v_pk_add_f32 v[144:145], s[6:7], v[144:145]
	v_and_b32_e32 v121, 0xffff0000, v121
	v_add_f32_e32 v109, v144, v145
	v_mov_b32_e32 v144, 0x358637bd
	s_nop 0
	v_fmac_f32_e32 v144, 0x3a800000, v109
	v_rsq_f32_e32 v144, v144
	v_mov_b32_e32 v109, v143
	v_add_u32_e32 v143, s4, v139
	s_addk_i32 s4, 0x1020
	v_pk_mul_f32 v[110:111], v[144:145], v[110:111] op_sel_hi:[0,1]
	v_pk_fma_f32 v[102:103], v[70:71], v[110:111], v[102:103]
	v_mov_b32_e32 v110, v124
	v_mov_b32_e32 v111, v126
	v_pk_mul_f32 v[110:111], v[144:145], v[110:111] op_sel_hi:[0,1]
	v_pk_fma_f32 v[110:111], v[74:75], v[110:111], v[106:107]
	v_pk_mul_f32 v[106:107], v[144:145], v[132:133] op_sel_hi:[0,1]
	v_pk_fma_f32 v[106:107], v[76:77], v[106:107], v[122:123]
	v_pk_mul_f32 v[122:123], v[108:109], v[144:145] op_sel_hi:[1,0]
	v_pk_mul_f32 v[108:109], v[114:115], v[144:145] op_sel_hi:[1,0]
	v_pk_fma_f32 v[114:115], v[82:83], v[122:123], v[118:119]
	v_bfe_u32 v118, v102, 16, 1
	v_pk_mul_f32 v[128:129], v[144:145], v[128:129] op_sel_hi:[0,1]
	v_add3_u32 v118, v102, v118, s15
	v_bfe_u32 v119, v103, 16, 1
	v_pk_fma_f32 v[100:101], v[68:69], v[128:129], v[100:101]
	v_lshrrev_b32_e32 v118, 16, v118
	v_add3_u32 v119, v103, v119, s15
	v_and_or_b32 v118, v119, s16, v118
	v_bfe_u32 v119, v100, 16, 1
	v_pk_fma_f32 v[108:109], v[80:81], v[108:109], v[120:121]
	v_add3_u32 v119, v100, v119, s15
	v_bfe_u32 v120, v101, 16, 1
	v_lshrrev_b32_e32 v119, 16, v119
	v_add3_u32 v120, v101, v120, s15
	v_mov_b32_e32 v126, v125
	v_and_or_b32 v119, v120, s16, v119
	v_bfe_u32 v120, v110, 16, 1
	v_pk_mul_f32 v[124:125], v[144:145], v[126:127] op_sel_hi:[0,1]
	v_add3_u32 v120, v110, v120, s15
	v_bfe_u32 v121, v111, 16, 1
	v_pk_fma_f32 v[104:105], v[72:73], v[124:125], v[104:105]
	v_lshrrev_b32_e32 v120, 16, v120
	v_add3_u32 v121, v111, v121, s15
	v_and_or_b32 v120, v121, s16, v120
	v_bfe_u32 v121, v104, 16, 1
	v_add3_u32 v121, v104, v121, s15
	v_bfe_u32 v122, v105, 16, 1
	v_pk_mul_f32 v[124:125], v[144:145], v[130:131] op_sel_hi:[0,1]
	v_lshrrev_b32_e32 v121, 16, v121
	v_add3_u32 v122, v105, v122, s15
	v_pk_fma_f32 v[112:113], v[78:79], v[124:125], v[112:113]
	v_and_or_b32 v121, v122, s16, v121
	global_store_dwordx4 v[116:117], v[118:121], off
	v_bfe_u32 v122, v109, 16, 1
	v_add3_u32 v122, v109, v122, s15
	v_bfe_u32 v118, v112, 16, 1
	v_add3_u32 v118, v112, v118, s15
; #define LAS __attribute__((address_space(3)))
; DI unsigned pk2(float lo, float hi) { return f2bf(lo) | (f2bf(hi) << 16); }
; DI unsigned pk_fp8x4(float a, float b, float c, float d) { int p = 0; p = __builtin_amdgcn_cvt_pk_fp8_f32(a, b, p, false); p = __builtin_amdgcn_cvt_pk_fp8_f32(c, d, p, true); return (unsigned)p; }
; DI void phase_tail(const Frame& F, int l) {
;     ...
;             { const float rs2 = rms_rstd(x);
; #pragma unroll
;               for (int j = 0; j < 4; ++j) hv[j] = x[j] * rs2 * Av[j] + Sv[j];
; #pragma unroll
;               for (int g = 0; g < 2; ++g) { u32x2 w; w.x = pk_fp8x4(hv[2 * g].x, hv[2 * g].y, hv[2 * g].z, hv[2 * g].w); w.y = pk_fp8x4(hv[2 * g + 1].x, hv[2 * g + 1].y, hv[2 * g + 1].z, hv[2 * g + 1].w);
;                   *(u32x2*)((unsigned char*)(F.ws + WS_H8) + (size_t)t * D + 8 * F.lane + 512 * g) = w; } }
; #pragma unroll
;             for (int g = 0; g < 2; ++g) { u32x4 w; w.x = pk2(hv[2 * g].x, hv[2 * g].y); w.y = pk2(hv[2 * g].z, hv[2 * g].w); w.z = pk2(hv[2 * g + 1].x, hv[2 * g + 1].y); w.w = pk2(hv[2 * g + 1].z, hv[2 * g + 1].w);
;                 *(LAS u32x4*)(Ht + tkl * HT_STRIDE + 8 * F.lane + 512 * g) = w; }
	v_bfe_u32 v119, v113, 16, 1
	v_lshrrev_b32_e32 v118, 16, v118
	v_add3_u32 v119, v113, v119, s15
	v_and_or_b32 v118, v119, s16, v118
	v_bfe_u32 v119, v106, 16, 1
	v_add3_u32 v119, v106, v119, s15
	v_bfe_u32 v120, v107, 16, 1
	v_lshrrev_b32_e32 v119, 16, v119
	v_add3_u32 v120, v107, v120, s15
	v_and_or_b32 v119, v120, s16, v119
	v_bfe_u32 v120, v114, 16, 1
	v_add3_u32 v120, v114, v120, s15
	v_bfe_u32 v121, v115, 16, 1
	v_lshrrev_b32_e32 v120, 16, v120
	v_add3_u32 v121, v115, v121, s15
	v_and_or_b32 v120, v121, s16, v120
	v_bfe_u32 v121, v108, 16, 1
	v_add3_u32 v121, v108, v121, s15
	v_lshrrev_b32_e32 v121, 16, v121
	v_and_or_b32 v121, v122, s16, v121
	global_store_dwordx4 v[116:117], v[118:121], off offset:1024
	v_pk_mul_f32 v[116:117], v[100:101], v[100:101]
	s_nop 0
	v_pk_mul_f32 v[118:119], v[102:103], v[102:103]
	s_nop 0
	v_pk_mov_b32 v[120:121], v[118:119], v[116:117] op_sel:[1,0]
	v_mov_b32_e32 v119, v117
	v_pk_add_f32 v[116:117], v[120:121], v[118:119]
	v_pk_mul_f32 v[118:119], v[104:105], v[104:105]
	v_pk_add_f32 v[116:117], v[116:117], v[116:117] op_sel_hi:[0,1]
	v_pk_mul_f32 v[120:121], v[110:111], v[110:111]
	v_mul_f32_e32 v116, v112, v112
	v_pk_mov_b32 v[122:123], v[120:121], v[118:119] op_sel:[1,0]
	v_mov_b32_e32 v121, v119
	v_pk_add_f32 v[118:119], v[122:123], v[120:121]
	v_pk_fma_f32 v[120:121], v[112:113], v[112:113], v[116:117] op_sel_hi:[1,1,0]
	v_mul_f32_e32 v116, v106, v106
	v_pk_add_f32 v[118:119], v[118:119], v[118:119] op_sel_hi:[0,1]
	v_pk_fma_f32 v[122:123], v[106:107], v[106:107], v[116:117] op_sel_hi:[1,1,0]
	v_mul_f32_e32 v120, v114, v114
	v_mul_f32_e32 v122, v115, v115
	v_mul_f32_e32 v116, v108, v108
	v_mul_f32_e32 v118, v109, v109
	v_pk_add_f32 v[120:121], v[120:121], v[122:123]
	v_pk_add_f32 v[116:117], v[116:117], v[118:119]
	s_nop 0
	v_pk_add_f32 v[116:117], v[120:121], v[116:117]
	s_nop 0
	v_add_f32_e32 v116, v116, v117
	s_nop 1
	v_add_f32_dpp v116, v116, v116 quad_perm:[1,0,3,2] row_mask:0xf bank_mask:0xf bound_ctrl:1
	s_nop 1
	v_add_f32_dpp v116, v116, v116 quad_perm:[2,3,0,1] row_mask:0xf bank_mask:0xf bound_ctrl:1
	s_nop 1
	v_add_f32_dpp v116, v116, v116 row_half_mirror row_mask:0xf bank_mask:0xf bound_ctrl:1
	s_nop 1
	v_add_f32_dpp v116, v116, v116 row_mirror row_mask:0xf bank_mask:0xf bound_ctrl:1
	s_nop 0
	v_readlane_b32 s2, v116, 16
	v_readlane_b32 s5, v116, 48
	v_readlane_b32 s6, v116, 0
	v_readlane_b32 s7, v116, 32
	v_mov_b32_e32 v116, s2
	v_mov_b32_e32 v117, s5
	v_pk_add_f32 v[116:117], s[6:7], v[116:117]
	s_lshl_b64 s[6:7], s[46:47], 11
	v_add_f32_e32 v116, v116, v117
	v_mov_b32_e32 v117, 0x358637bd
	s_add_i32 s46, s46, 2
	v_fmac_f32_e32 v117, 0x3a800000, v116
	v_rsq_f32_e32 v116, v117
	s_cmpk_eq_i32 s4, 0x2040
	v_pk_mul_f32 v[100:101], v[100:101], v[116:117] op_sel_hi:[1,0]
	v_pk_mul_f32 v[102:103], v[102:103], v[116:117] op_sel_hi:[1,0]
	v_pk_fma_f32 v[118:119], v[84:85], v[100:101], v[6:7]
	v_pk_mul_f32 v[100:101], v[110:111], v[116:117] op_sel_hi:[1,0]
	v_pk_fma_f32 v[120:121], v[86:87], v[102:103], v[4:5]
	v_pk_mul_f32 v[102:103], v[104:105], v[116:117] op_sel_hi:[1,0]
	v_pk_fma_f32 v[110:111], v[90:91], v[100:101], v[0:1]
	v_pk_mul_f32 v[100:101], v[112:113], v[116:117] op_sel_hi:[1,0]
	v_pk_fma_f32 v[122:123], v[88:89], v[102:103], v[2:3]
	v_pk_mul_f32 v[102:103], v[106:107], v[116:117] op_sel_hi:[1,0]
	v_pk_fma_f32 v[106:107], v[94:95], v[100:101], v[12:13]
	v_pk_mul_f32 v[100:101], v[108:109], v[116:117] op_sel_hi:[1,0]
	v_mov_b32_e32 v108, v193
	v_mov_b32_e32 v109, v193
	v_cvt_pk_fp8_f32 v108, v120, v121
	v_cvt_pk_fp8_f32 v109, v110, v111
	v_lshl_add_u64 v[112:113], s[54:55], 0, v[64:65]
	v_add_co_u32_e32 v112, vcc, s18, v112
	v_cvt_pk_fp8_f32 v108, v118, v119 op_sel:[0,0,1]
	v_cvt_pk_fp8_f32 v109, v122, v123 op_sel:[0,0,1]
	v_pk_fma_f32 v[104:105], v[92:93], v[102:103], v[14:15]
	v_pk_mul_f32 v[102:103], v[114:115], v[116:117] op_sel_hi:[1,0]
	v_addc_co_u32_e32 v113, vcc, 0, v113, vcc
	v_pk_fma_f32 v[102:103], v[98:99], v[102:103], v[8:9]
	global_store_dwordx2 v[112:113], v[108:109], off
	v_mov_b32_e32 v108, v193
	v_mov_b32_e32 v109, v193
	v_cvt_pk_fp8_f32 v108, v106, v107
	v_cvt_pk_fp8_f32 v109, v102, v103
	v_pk_fma_f32 v[100:101], v[96:97], v[100:101], v[10:11]
	v_lshl_add_u64 v[116:117], v[56:57], 0, s[6:7]
	v_cvt_pk_fp8_f32 v108, v104, v105 op_sel:[0,0,1]
	v_cvt_pk_fp8_f32 v109, v100, v101 op_sel:[0,0,1]
	v_lshl_add_u64 v[64:65], v[64:65], 0, s[34:35]
	global_store_dwordx2 v[112:113], v[108:109], off offset:512
	v_bfe_u32 v108, v120, 16, 1
	v_add3_u32 v108, v120, v108, s15
	v_bfe_u32 v109, v121, 16, 1
	v_lshrrev_b32_e32 v108, 16, v108
	v_add3_u32 v109, v121, v109, s15
	v_and_or_b32 v108, v109, s16, v108
	v_bfe_u32 v109, v118, 16, 1
	v_add3_u32 v109, v118, v109, s15
	v_bfe_u32 v112, v119, 16, 1
	v_lshrrev_b32_e32 v109, 16, v109
	v_add3_u32 v112, v119, v112, s15
	v_and_or_b32 v109, v112, s16, v109
	v_bfe_u32 v112, v110, 16, 1
	v_add3_u32 v110, v110, v112, s15
	v_bfe_u32 v112, v111, 16, 1
	v_lshrrev_b32_e32 v110, 16, v110
	v_add3_u32 v111, v111, v112, s15
	v_and_or_b32 v110, v111, s16, v110
	v_bfe_u32 v111, v122, 16, 1
	v_add3_u32 v111, v122, v111, s15
	v_bfe_u32 v112, v123, 16, 1
	v_lshrrev_b32_e32 v111, 16, v111
	v_add3_u32 v112, v123, v112, s15
	v_and_or_b32 v111, v112, s16, v111
	ds_write_b128 v143, v[108:111]
	v_bfe_u32 v108, v106, 16, 1
	v_add3_u32 v106, v106, v108, s15
	v_bfe_u32 v108, v107, 16, 1
	v_lshrrev_b32_e32 v106, 16, v106
	v_add3_u32 v107, v107, v108, s15
	v_and_or_b32 v106, v107, s16, v106
	v_bfe_u32 v107, v104, 16, 1
	v_add3_u32 v104, v104, v107, s15
	v_bfe_u32 v107, v105, 16, 1
	v_lshrrev_b32_e32 v104, 16, v104
	v_add3_u32 v105, v105, v107, s15
	v_and_or_b32 v107, v105, s16, v104
	v_bfe_u32 v104, v102, 16, 1
	v_add3_u32 v102, v102, v104, s15
	v_bfe_u32 v104, v103, 16, 1
	v_lshrrev_b32_e32 v102, 16, v102
	v_add3_u32 v103, v103, v104, s15
	v_and_or_b32 v108, v103, s16, v102
	v_bfe_u32 v102, v100, 16, 1
	v_add3_u32 v100, v100, v102, s15
	v_bfe_u32 v102, v101, 16, 1
	v_lshrrev_b32_e32 v100, 16, v100
	v_add3_u32 v101, v101, v102, s15
	v_and_or_b32 v109, v101, s16, v100
	ds_write_b128 v143, v[106:109] offset:1024
	v_lshl_add_u64 v[100:101], v[54:55], 0, s[6:7]
	s_waitcnt vmcnt(12)
; #define LAS __attribute__((address_space(3)))
; DI unsigned pk2(float lo, float hi) { return f2bf(lo) | (f2bf(hi) << 16); }
; DI unsigned pk_fp8x4(float a, float b, float c, float d) { int p = 0; p = __builtin_amdgcn_cvt_pk_fp8_f32(a, b, p, false); p = __builtin_amdgcn_cvt_pk_fp8_f32(c, d, p, true); return (unsigned)p; }
; DI void phase_tail(const Frame& F, int l) {
;     ...
;         for (int q = 0; q < 4; ++q) {
;             const int tkl = 4 * F.wave + q, t = 32 * ti + tkl;
;             f32x4 y[4], x[4], hv[4];
;             load_bf16_row((const bf16_t*)(F.ws + WS_Y) + (size_t)t * D, F.lane, y);
;             load_bf16_row((const bf16_t*)(F.ws + WS_XB) + (size_t)t * D, F.lane, x);
;             const float rstd = rms_rstd(y);
; #pragma unroll
;             for (int j = 0; j < 4; ++j) x[j] = x[j] + Bv[j] * (y[j] * rstd);
;             store_bf16_row((bf16_t*)(F.ws + WS_XB) + (size_t)t * D, F.lane, x);
;             { const float rs2 = rms_rstd(x);
; #pragma unroll
;               for (int j = 0; j < 4; ++j) hv[j] = x[j] * rs2 * Av[j] + Sv[j];
; #pragma unroll
;               for (int g = 0; g < 2; ++g) { u32x2 w; w.x = pk_fp8x4(hv[2 * g].x, hv[2 * g].y, hv[2 * g].z, hv[2 * g].w); w.y = pk_fp8x4(hv[2 * g + 1].x, hv[2 * g + 1].y, hv[2 * g + 1].z, hv[2 * g + 1].w);
;                   *(u32x2*)((unsigned char*)(F.ws + WS_H8) + (size_t)t * D + 8 * F.lane + 512 * g) = w; } }
; #pragma unroll
;             for (int g = 0; g < 2; ++g) { u32x4 w; w.x = pk2(hv[2 * g].x, hv[2 * g].y); w.y = pk2(hv[2 * g].z, hv[2 * g].w); w.z = pk2(hv[2 * g + 1].x, hv[2 * g + 1].y); w.w = pk2(hv[2 * g + 1].z, hv[2 * g + 1].w);
;                 *(LAS u32x4*)(Ht + tkl * HT_STRIDE + 8 * F.lane + 512 * g) = w; }
	v_mov_b32_e32 v124, v160
	v_mov_b32_e32 v125, v161
	v_mov_b32_e32 v126, v162
	v_mov_b32_e32 v127, v163
	v_mov_b32_e32 v144, v164
	v_mov_b32_e32 v145, v165
	v_mov_b32_e32 v146, v166
	v_mov_b32_e32 v147, v167
	v_mov_b32_e32 v110, v168
	v_mov_b32_e32 v111, v169
	v_mov_b32_e32 v112, v170
	v_mov_b32_e32 v113, v171
	v_mov_b32_e32 v118, v172
	v_mov_b32_e32 v119, v173
	v_mov_b32_e32 v120, v174
	v_mov_b32_e32 v121, v175
	v_lshlrev_b32_e32 v128, 16, v125
	v_lshlrev_b32_e32 v108, 16, v146
	v_lshlrev_b32_e32 v102, 16, v110
	v_and_b32_e32 v103, 0xffff0000, v110
	v_lshlrev_b32_e32 v110, 16, v124
	v_lshlrev_b32_e32 v100, 16, v111
	v_and_b32_e32 v101, 0xffff0000, v111
	v_and_b32_e32 v111, 0xffff0000, v124
	v_mul_f32_e32 v124, v110, v110
	v_and_b32_e32 v156, 0xffff0000, v146
	v_lshlrev_b32_e32 v114, 16, v147
	v_and_b32_e32 v115, 0xffff0000, v147
	v_pk_fma_f32 v[146:147], v[110:111], v[110:111], v[124:125] op_sel_hi:[1,1,0]
	v_and_b32_e32 v129, 0xffff0000, v125
	v_mul_f32_e32 v124, v128, v128
	v_pk_fma_f32 v[148:149], v[128:129], v[128:129], v[124:125] op_sel_hi:[1,1,0]
	v_lshlrev_b32_e32 v125, 16, v127
	v_lshlrev_b32_e32 v124, 16, v126
	v_and_b32_e32 v127, 0xffff0000, v127
	v_and_b32_e32 v126, 0xffff0000, v126
	v_pk_mul_f32 v[130:131], v[126:127], v[126:127]
	v_mov_b32_e32 v109, v147
	v_pk_fma_f32 v[130:131], v[124:125], v[124:125], v[130:131]
	v_mov_b32_e32 v154, v108
	v_pk_add_f32 v[150:151], v[130:131], v[130:131] op_sel_hi:[0,1]
	v_lshlrev_b32_e32 v130, 16, v144
	v_and_b32_e32 v131, 0xffff0000, v144
	v_mul_f32_e32 v132, v130, v130
	v_pk_fma_f32 v[152:153], v[130:131], v[130:131], v[132:133] op_sel_hi:[1,1,0]
	v_lshlrev_b32_e32 v132, 16, v145
	v_and_b32_e32 v133, 0xffff0000, v145
	v_mul_f32_e32 v144, v132, v132
	v_mov_b32_e32 v155, v149
	v_pk_fma_f32 v[144:145], v[132:133], v[132:133], v[144:145] op_sel_hi:[1,1,0]
	v_pk_mul_f32 v[154:155], v[108:109], v[154:155]
	v_pk_add_f32 v[146:147], v[146:147], v[148:149]
	v_mul_f32_e32 v150, v156, v156
	v_mul_f32_e32 v152, v114, v114
	v_mul_f32_e32 v144, v115, v115
	v_mov_b32_e32 v155, v147
	v_pk_add_f32 v[146:147], v[154:155], v[150:151]
	v_pk_add_f32 v[144:145], v[152:153], v[144:145]
	v_lshlrev_b32_e32 v106, 16, v112
	v_pk_add_f32 v[144:145], v[146:147], v[144:145]
	v_and_b32_e32 v107, 0xffff0000, v112
	v_add_f32_e32 v109, v144, v145
	v_lshlrev_b32_e32 v122, 16, v119
	v_and_b32_e32 v123, 0xffff0000, v119
	v_add_f32_dpp v109, v109, v109 quad_perm:[1,0,3,2] row_mask:0xf bank_mask:0xf bound_ctrl:1
	v_lshlrev_b32_e32 v104, 16, v113
	v_and_b32_e32 v105, 0xffff0000, v113
	v_add_f32_dpp v109, v109, v109 quad_perm:[2,3,0,1] row_mask:0xf bank_mask:0xf bound_ctrl:1
	v_lshlrev_b32_e32 v112, 16, v118
	v_and_b32_e32 v113, 0xffff0000, v118
	v_add_f32_dpp v109, v109, v109 row_half_mirror row_mask:0xf bank_mask:0xf bound_ctrl:1
	v_lshlrev_b32_e32 v118, 16, v120
	v_and_b32_e32 v119, 0xffff0000, v120
	v_add_f32_dpp v109, v109, v109 row_mirror row_mask:0xf bank_mask:0xf bound_ctrl:1
	v_lshlrev_b32_e32 v120, 16, v121
	v_readlane_b32 s2, v109, 16
	v_readlane_b32 s5, v109, 48
	v_readlane_b32 s6, v109, 0
	v_readlane_b32 s7, v109, 32
	v_mov_b32_e32 v144, s2
	v_mov_b32_e32 v145, s5
	v_pk_add_f32 v[144:145], s[6:7], v[144:145]
	v_and_b32_e32 v121, 0xffff0000, v121
	v_add_f32_e32 v109, v144, v145
	v_mov_b32_e32 v144, 0x358637bd
	s_nop 0
	v_fmac_f32_e32 v144, 0x3a800000, v109
	v_rsq_f32_e32 v144, v144
	v_mov_b32_e32 v109, v156
	v_pk_mul_f32 v[110:111], v[144:145], v[110:111] op_sel_hi:[0,1]
	v_pk_fma_f32 v[102:103], v[70:71], v[110:111], v[102:103]
	v_mov_b32_e32 v110, v124
	v_mov_b32_e32 v111, v126
	v_pk_mul_f32 v[110:111], v[144:145], v[110:111] op_sel_hi:[0,1]
	v_pk_fma_f32 v[110:111], v[74:75], v[110:111], v[106:107]
	v_pk_mul_f32 v[106:107], v[144:145], v[132:133] op_sel_hi:[0,1]
	v_pk_fma_f32 v[106:107], v[76:77], v[106:107], v[122:123]
	v_pk_mul_f32 v[122:123], v[108:109], v[144:145] op_sel_hi:[1,0]
	v_pk_mul_f32 v[108:109], v[114:115], v[144:145] op_sel_hi:[1,0]
	v_pk_fma_f32 v[114:115], v[82:83], v[122:123], v[118:119]
	v_bfe_u32 v118, v102, 16, 1
	v_pk_mul_f32 v[128:129], v[144:145], v[128:129] op_sel_hi:[0,1]
	v_add3_u32 v118, v102, v118, s15
	v_bfe_u32 v119, v103, 16, 1
	v_pk_fma_f32 v[100:101], v[68:69], v[128:129], v[100:101]
	v_lshrrev_b32_e32 v118, 16, v118
	v_add3_u32 v119, v103, v119, s15
	v_and_or_b32 v118, v119, s16, v118
	v_bfe_u32 v119, v100, 16, 1
	v_pk_fma_f32 v[108:109], v[80:81], v[108:109], v[120:121]
	v_add3_u32 v119, v100, v119, s15
	v_bfe_u32 v120, v101, 16, 1
	v_lshrrev_b32_e32 v119, 16, v119
	v_add3_u32 v120, v101, v120, s15
	v_mov_b32_e32 v126, v125
	v_and_or_b32 v119, v120, s16, v119
	v_bfe_u32 v120, v110, 16, 1
	v_pk_mul_f32 v[124:125], v[144:145], v[126:127] op_sel_hi:[0,1]
	v_add3_u32 v120, v110, v120, s15
	v_bfe_u32 v121, v111, 16, 1
	v_pk_fma_f32 v[104:105], v[72:73], v[124:125], v[104:105]
	v_lshrrev_b32_e32 v120, 16, v120
	v_add3_u32 v121, v111, v121, s15
	v_and_or_b32 v120, v121, s16, v120
	v_bfe_u32 v121, v104, 16, 1
	v_add3_u32 v121, v104, v121, s15
	v_bfe_u32 v122, v105, 16, 1
	v_pk_mul_f32 v[124:125], v[144:145], v[130:131] op_sel_hi:[0,1]
	v_lshrrev_b32_e32 v121, 16, v121
	v_add3_u32 v122, v105, v122, s15
	v_pk_fma_f32 v[112:113], v[78:79], v[124:125], v[112:113]
	v_and_or_b32 v121, v122, s16, v121
	global_store_dwordx4 v[116:117], v[118:121], off
	v_bfe_u32 v122, v109, 16, 1
	v_add3_u32 v122, v109, v122, s15
	v_bfe_u32 v118, v112, 16, 1
	v_add3_u32 v118, v112, v118, s15
	v_bfe_u32 v119, v113, 16, 1
	v_lshrrev_b32_e32 v118, 16, v118
	v_add3_u32 v119, v113, v119, s15
	v_and_or_b32 v118, v119, s16, v118
	v_bfe_u32 v119, v106, 16, 1
	v_add3_u32 v119, v106, v119, s15
	v_bfe_u32 v120, v107, 16, 1
; #define LAS __attribute__((address_space(3)))
; DI unsigned pk2(float lo, float hi) { return f2bf(lo) | (f2bf(hi) << 16); }
; DI unsigned pk_fp8x4(float a, float b, float c, float d) { int p = 0; p = __builtin_amdgcn_cvt_pk_fp8_f32(a, b, p, false); p = __builtin_amdgcn_cvt_pk_fp8_f32(c, d, p, true); return (unsigned)p; }
; DI void phase_tail(const Frame& F, int l) {
;     ...
;             { const float rs2 = rms_rstd(x);
; #pragma unroll
;               for (int j = 0; j < 4; ++j) hv[j] = x[j] * rs2 * Av[j] + Sv[j];
; #pragma unroll
;               for (int g = 0; g < 2; ++g) { u32x2 w; w.x = pk_fp8x4(hv[2 * g].x, hv[2 * g].y, hv[2 * g].z, hv[2 * g].w); w.y = pk_fp8x4(hv[2 * g + 1].x, hv[2 * g + 1].y, hv[2 * g + 1].z, hv[2 * g + 1].w);
;                   *(u32x2*)((unsigned char*)(F.ws + WS_H8) + (size_t)t * D + 8 * F.lane + 512 * g) = w; } }
; #pragma unroll
;             for (int g = 0; g < 2; ++g) { u32x4 w; w.x = pk2(hv[2 * g].x, hv[2 * g].y); w.y = pk2(hv[2 * g].z, hv[2 * g].w); w.z = pk2(hv[2 * g + 1].x, hv[2 * g + 1].y); w.w = pk2(hv[2 * g + 1].z, hv[2 * g + 1].w);
;                 *(LAS u32x4*)(Ht + tkl * HT_STRIDE + 8 * F.lane + 512 * g) = w; }
	v_lshrrev_b32_e32 v119, 16, v119
	v_add3_u32 v120, v107, v120, s15
	v_and_or_b32 v119, v120, s16, v119
	v_bfe_u32 v120, v114, 16, 1
	v_add3_u32 v120, v114, v120, s15
	v_bfe_u32 v121, v115, 16, 1
	v_lshrrev_b32_e32 v120, 16, v120
	v_add3_u32 v121, v115, v121, s15
	v_and_or_b32 v120, v121, s16, v120
	v_bfe_u32 v121, v108, 16, 1
	v_add3_u32 v121, v108, v121, s15
	v_lshrrev_b32_e32 v121, 16, v121
	v_and_or_b32 v121, v122, s16, v121
	global_store_dwordx4 v[116:117], v[118:121], off offset:1024
	v_pk_mul_f32 v[116:117], v[100:101], v[100:101]
	s_nop 0
	v_pk_mul_f32 v[118:119], v[102:103], v[102:103]
	s_nop 0
	v_pk_mov_b32 v[120:121], v[118:119], v[116:117] op_sel:[1,0]
	v_mov_b32_e32 v119, v117
	v_pk_add_f32 v[116:117], v[120:121], v[118:119]
	v_pk_mul_f32 v[118:119], v[104:105], v[104:105]
	v_pk_add_f32 v[116:117], v[116:117], v[116:117] op_sel_hi:[0,1]
	v_pk_mul_f32 v[120:121], v[110:111], v[110:111]
	v_mul_f32_e32 v116, v112, v112
	v_pk_mov_b32 v[122:123], v[120:121], v[118:119] op_sel:[1,0]
	v_mov_b32_e32 v121, v119
	v_pk_add_f32 v[118:119], v[122:123], v[120:121]
	v_pk_fma_f32 v[120:121], v[112:113], v[112:113], v[116:117] op_sel_hi:[1,1,0]
	v_mul_f32_e32 v116, v106, v106
	v_pk_add_f32 v[118:119], v[118:119], v[118:119] op_sel_hi:[0,1]
	v_pk_fma_f32 v[122:123], v[106:107], v[106:107], v[116:117] op_sel_hi:[1,1,0]
	v_mul_f32_e32 v120, v114, v114
	v_mul_f32_e32 v122, v115, v115
	v_mul_f32_e32 v116, v108, v108
	v_mul_f32_e32 v118, v109, v109
	v_pk_add_f32 v[120:121], v[120:121], v[122:123]
	v_pk_add_f32 v[116:117], v[116:117], v[118:119]
	s_nop 0
	v_pk_add_f32 v[116:117], v[120:121], v[116:117]
	s_nop 0
	v_add_f32_e32 v116, v116, v117
	s_nop 1
	v_add_f32_dpp v116, v116, v116 quad_perm:[1,0,3,2] row_mask:0xf bank_mask:0xf bound_ctrl:1
	s_nop 1
	v_add_f32_dpp v116, v116, v116 quad_perm:[2,3,0,1] row_mask:0xf bank_mask:0xf bound_ctrl:1
	s_nop 1
	v_add_f32_dpp v116, v116, v116 row_half_mirror row_mask:0xf bank_mask:0xf bound_ctrl:1
	s_nop 1
	v_add_f32_dpp v116, v116, v116 row_mirror row_mask:0xf bank_mask:0xf bound_ctrl:1
	s_nop 0
	v_readlane_b32 s2, v116, 16
	v_readlane_b32 s5, v116, 48
	v_readlane_b32 s6, v116, 0
	v_readlane_b32 s7, v116, 32
	v_mov_b32_e32 v116, s2
	v_mov_b32_e32 v117, s5
	v_pk_add_f32 v[116:117], s[6:7], v[116:117]
	s_nop 0
	v_add_f32_e32 v116, v116, v117
	v_mov_b32_e32 v117, 0x358637bd
	s_nop 0
	v_fmac_f32_e32 v117, 0x3a800000, v116
	v_rsq_f32_e32 v116, v117
	s_nop 0
	v_pk_mul_f32 v[102:103], v[102:103], v[116:117] op_sel_hi:[1,0]
	v_pk_mul_f32 v[100:101], v[100:101], v[116:117] op_sel_hi:[1,0]
	v_pk_mul_f32 v[104:105], v[104:105], v[116:117] op_sel_hi:[1,0]
	v_pk_fma_f32 v[118:119], v[84:85], v[100:101], v[6:7]
	v_pk_fma_f32 v[100:101], v[86:87], v[102:103], v[4:5]
	v_pk_mul_f32 v[102:103], v[110:111], v[116:117] op_sel_hi:[1,0]
	v_pk_mul_f32 v[110:111], v[112:113], v[116:117] op_sel_hi:[1,0]
	v_pk_fma_f32 v[102:103], v[90:91], v[102:103], v[0:1]
	v_pk_mul_f32 v[112:113], v[114:115], v[116:117] op_sel_hi:[1,0]
	v_mov_b32_e32 v114, v193
	v_mov_b32_e32 v115, v193
	v_cvt_pk_fp8_f32 v114, v100, v101
	v_cvt_pk_fp8_f32 v115, v102, v103
	v_pk_fma_f32 v[104:105], v[88:89], v[104:105], v[2:3]
	v_pk_mul_f32 v[106:107], v[106:107], v[116:117] op_sel_hi:[1,0]
	v_cvt_pk_fp8_f32 v114, v118, v119 op_sel:[0,0,1]
	v_cvt_pk_fp8_f32 v115, v104, v105 op_sel:[0,0,1]
	v_pk_mul_f32 v[108:109], v[108:109], v[116:117] op_sel_hi:[1,0]
	v_lshl_add_u64 v[116:117], v[60:61], 0, s[66:67]
	v_pk_fma_f32 v[110:111], v[94:95], v[110:111], v[12:13]
	v_pk_fma_f32 v[112:113], v[98:99], v[112:113], v[8:9]
	global_store_dwordx2 v[116:117], v[114:115], off
	v_mov_b32_e32 v114, v193
	v_mov_b32_e32 v115, v193
	v_cvt_pk_fp8_f32 v114, v110, v111
	v_cvt_pk_fp8_f32 v115, v112, v113
	v_pk_fma_f32 v[106:107], v[92:93], v[106:107], v[14:15]
	v_pk_fma_f32 v[108:109], v[96:97], v[108:109], v[10:11]
	v_cvt_pk_fp8_f32 v114, v106, v107 op_sel:[0,0,1]
	v_cvt_pk_fp8_f32 v115, v108, v109 op_sel:[0,0,1]
	v_lshl_add_u64 v[116:117], v[58:59], 0, s[66:67]
	v_add_co_u32_e32 v116, vcc, s18, v116
	s_nop 1
	v_addc_co_u32_e32 v117, vcc, 0, v117, vcc
	global_store_dwordx2 v[116:117], v[114:115], off offset:512
	v_bfe_u32 v114, v100, 16, 1
	v_add3_u32 v100, v100, v114, s15
	v_bfe_u32 v114, v101, 16, 1
	v_lshrrev_b32_e32 v100, 16, v100
	v_add3_u32 v101, v101, v114, s15
	v_and_or_b32 v100, v101, s16, v100
	v_bfe_u32 v101, v118, 16, 1
	v_add3_u32 v101, v118, v101, s15
	v_bfe_u32 v114, v119, 16, 1
	v_lshrrev_b32_e32 v101, 16, v101
	v_add3_u32 v114, v119, v114, s15
	v_and_or_b32 v101, v114, s16, v101
	v_bfe_u32 v114, v102, 16, 1
	v_add3_u32 v102, v102, v114, s15
	v_bfe_u32 v114, v103, 16, 1
	v_lshrrev_b32_e32 v102, 16, v102
	v_add3_u32 v103, v103, v114, s15
	v_and_or_b32 v102, v103, s16, v102
	v_bfe_u32 v103, v104, 16, 1
	v_add3_u32 v103, v104, v103, s15
	v_bfe_u32 v104, v105, 16, 1
	v_lshrrev_b32_e32 v103, 16, v103
	v_add3_u32 v104, v105, v104, s15
	v_and_or_b32 v103, v104, s16, v103
	ds_write_b128 v143, v[100:103] offset:2064
	v_bfe_u32 v100, v110, 16, 1
	v_add3_u32 v100, v110, v100, s15
	v_bfe_u32 v101, v111, 16, 1
	v_lshrrev_b32_e32 v100, 16, v100
	v_add3_u32 v101, v111, v101, s15
	v_and_or_b32 v100, v101, s16, v100
	v_bfe_u32 v101, v106, 16, 1
	v_add3_u32 v101, v106, v101, s15
	v_bfe_u32 v102, v107, 16, 1
	v_lshrrev_b32_e32 v101, 16, v101
	v_add3_u32 v102, v107, v102, s15
	v_and_or_b32 v101, v102, s16, v101
	v_bfe_u32 v102, v112, 16, 1
	v_add3_u32 v102, v112, v102, s15
	v_bfe_u32 v103, v113, 16, 1
	v_lshrrev_b32_e32 v102, 16, v102
	v_add3_u32 v103, v113, v103, s15
	v_and_or_b32 v102, v103, s16, v102
	v_bfe_u32 v103, v108, 16, 1
	v_add3_u32 v103, v108, v103, s15
	v_bfe_u32 v104, v109, 16, 1
	v_lshrrev_b32_e32 v103, 16, v103
	v_add3_u32 v104, v109, v104, s15
	v_and_or_b32 v103, v104, s16, v103
	ds_write_b128 v143, v[100:103] offset:3088
	s_cbranch_scc0 .LBB0_960
; #define LAS __attribute__((address_space(3)))
; DI void phase_tail(const Frame& F, int l) {
;     ...
;         { f32x16 acc;
; #pragma unroll
;           for (int i = 0; i < 16; ++i) acc[i] = 0.f;
; #pragma unroll
;           for (int s = 0; s < 8; ++s) { const bf16x8 af = *(const LAS bf16x8*)(Ht + r * HT_STRIDE + 128 * F.wave + 16 * s + 8 * h);
;               acc = __builtin_amdgcn_mfma_f32_32x32x16_bf16(af, RWf[s], acc, 0, 0, 0); }
; #pragma unroll
;           for (int i = 0; i < 16; ++i) Pz[(F.wave * 32 + ((i & 3) + 8 * (i >> 2) + 4 * h)) * 32 + r] = acc[i]; }
;         __syncthreads();
	s_waitcnt lgkmcnt(0)
	s_barrier
	ds_read_b128 v[0:3], v141
	ds_read_b128 v[62:65], v141 offset:32
	ds_read_b128 v[100:103], v141 offset:64
	ds_read_b128 v[104:107], v141 offset:96
	ds_read_b128 v[108:111], v141 offset:128
	ds_read_b128 v[112:115], v141 offset:160
	ds_read_b128 v[116:119], v141 offset:192
	ds_read_b128 v[120:123], v141 offset:224
	s_lshl_b32 s10, s24, 5
	s_mov_b32 s2, 0
	s_mov_b64 s[66:67], -1
	v_add_u32_e32 v68, 0x400, v142
	s_waitcnt lgkmcnt(7)
	v_mfma_f32_32x32x16_bf16 v[0:15], v[0:3], v[16:19], 0
	v_add_u32_e32 v69, 0x800, v142
	v_add_u32_e32 v70, 0xc00, v142
	s_waitcnt lgkmcnt(6)
	v_mfma_f32_32x32x16_bf16 v[0:15], v[62:65], v[20:23], v[0:15]
	s_waitcnt lgkmcnt(5)
	v_mfma_f32_32x32x16_bf16 v[0:15], v[100:103], v[24:27], v[0:15]
	s_waitcnt lgkmcnt(4)
	v_mfma_f32_32x32x16_bf16 v[0:15], v[104:107], v[28:31], v[0:15]
	s_waitcnt lgkmcnt(3)
	v_mfma_f32_32x32x16_bf16 v[0:15], v[108:111], v[32:35], v[0:15]
	s_waitcnt lgkmcnt(2)
	v_mfma_f32_32x32x16_bf16 v[0:15], v[112:115], v[36:39], v[0:15]
	s_waitcnt lgkmcnt(1)
	v_mfma_f32_32x32x16_bf16 v[0:15], v[116:119], v[40:43], v[0:15]
	s_waitcnt lgkmcnt(0)
	v_mfma_f32_32x32x16_bf16 v[0:15], v[120:123], v[44:47], v[0:15]
	s_nop 11
	ds_write2_b32 v142, v0, v1 offset1:32
	ds_write2_b32 v142, v2, v3 offset0:64 offset1:96
	ds_write2_b32 v68, v4, v5 offset1:32
	ds_write2_b32 v68, v6, v7 offset0:64 offset1:96
	ds_write2_b32 v69, v8, v9 offset1:32
	ds_write2_b32 v69, v10, v11 offset0:64 offset1:96
	ds_write2_b32 v70, v12, v13 offset1:32
	ds_write2_b32 v70, v14, v15 offset0:64 offset1:96
	s_waitcnt lgkmcnt(0)
	s_barrier
	s_branch .LBB0_963
